# attention tile loops: waves 0-3 (instead of 4-7) delayed by s_sleep 2 after each tile barrier
# baseline (speedup 1.0000x reference)
.LBB0_1652:
	s_or_b64 exec, exec, s[8:9]
	s_barrier
	v_readfirstlane_b32 s101, v0
	s_bitcmp1_b32 s101, 8
	s_cbranch_scc1 .Lmy_stagA_ma
	s_sleep 2

.LBB0_1707:
	s_or_b64 exec, exec, s[34:35]
	s_barrier
	v_readfirstlane_b32 s101, v0
	s_bitcmp1_b32 s101, 8
	s_cbranch_scc1 .Lmy_stagA_dl
	s_sleep 2
